# peer_down loop: last A operand kept in its landing registers; the loop-latch copy and its two vmcnt waits (a drain of all gathers every trip) removed
# speedup vs baseline: 1.0007x; 1.0007x over previous
.LBB0_1198:
	v_readlane_b32 s4, v254, 12
	s_or_b32 s84, s14, s4
	v_lshl_or_b32 v2, s84, 7, v217
	v_mov_b32_e32 v3, v4
	v_lshl_add_u64 v[6:7], v[2:3], 2, s[8:9]
	global_load_dwordx2 v[184:185], v[6:7], off
	s_nop 0
	global_load_dwordx4 v[6:9], v[176:177], off
	global_load_dword v235, v[178:179], off
	s_waitcnt vmcnt(0)
	ds_bpermute_b32 v5, v216, v6
	ds_bpermute_b32 v58, v216, v7
	ds_bpermute_b32 v50, v216, v8
	ds_bpermute_b32 v51, v216, v9
	ds_bpermute_b32 v42, v222, v6
	ds_bpermute_b32 v43, v222, v7
	ds_bpermute_b32 v34, v222, v8
	s_waitcnt lgkmcnt(0)
	ds_bpermute_b32 v35, v222, v9
	ds_bpermute_b32 v26, v223, v6
	ds_bpermute_b32 v27, v223, v7
	ds_bpermute_b32 v18, v223, v8
	ds_bpermute_b32 v19, v223, v9
	ds_bpermute_b32 v10, v224, v6
	ds_bpermute_b32 v11, v224, v7
	ds_bpermute_b32 v12, v224, v8
	ds_bpermute_b32 v13, v224, v9
	s_andn2_b64 vcc, exec, s[10:11]
	s_cbranch_vccnz .LBB0_1197
	s_lshl_b64 s[14:15], s[84:85], 21
	s_add_u32 s14, s46, s14
	s_addc_u32 s15, s47, s15
	v_lshlrev_b32_e32 v14, 1, v2
	v_lshl_add_u64 v[188:189], v[2:3], 2, s[6:7]
	s_waitcnt lgkmcnt(0)
	v_lshl_or_b32 v2, v13, 7, v218
	v_readlane_b32 s16, v252, 45
	global_load_dwordx4 v[170:173], v2, s[14:15]
	v_lshl_or_b32 v2, v12, 7, v218
	v_mov_b32_e32 v15, v4
	v_readlane_b32 s17, v252, 46
	global_load_dwordx4 v[166:169], v2, s[14:15]
	v_lshl_or_b32 v2, v11, 7, v218
	v_lshl_add_u64 v[186:187], s[16:17], 0, v[14:15]
	global_load_dwordx4 v[14:17], v2, s[14:15]
	v_lshl_or_b32 v2, v10, 7, v218
	global_load_dwordx4 v[10:13], v2, s[14:15]
	v_lshl_or_b32 v2, v19, 7, v218
	global_load_dwordx4 v[22:25], v2, s[14:15]
	v_lshl_or_b32 v2, v18, 7, v218
	global_load_dwordx4 v[18:21], v2, s[14:15]
	v_lshl_or_b32 v2, v27, 7, v218
	global_load_dwordx4 v[30:33], v2, s[14:15]
	v_lshl_or_b32 v2, v26, 7, v218
	global_load_dwordx4 v[26:29], v2, s[14:15]
	v_lshl_or_b32 v2, v35, 7, v218
	global_load_dwordx4 v[38:41], v2, s[14:15]
	v_lshl_or_b32 v2, v34, 7, v218
	global_load_dwordx4 v[34:37], v2, s[14:15]
	v_lshl_or_b32 v2, v43, 7, v218
	global_load_dwordx4 v[46:49], v2, s[14:15]
	v_lshl_or_b32 v2, v42, 7, v218
	global_load_dwordx4 v[42:45], v2, s[14:15]
	v_lshl_or_b32 v2, v51, 7, v218
	global_load_dwordx4 v[54:57], v2, s[14:15]
	v_lshl_or_b32 v2, v50, 7, v218
	global_load_dwordx4 v[50:53], v2, s[14:15]
	v_lshl_or_b32 v2, v58, 7, v218
	global_load_dwordx4 v[62:65], v2, s[14:15]
	v_lshl_or_b32 v2, v5, 7, v218
	global_load_dwordx4 v[58:61], v2, s[14:15]
	s_mul_i32 s16, s84, 0x11000
	v_readlane_b32 s18, v254, 29
	v_readlane_b32 s19, v254, 30
	s_add_u32 s48, s18, s16
	s_addc_u32 s49, s19, 0
	s_mov_b32 s50, 0
	s_mov_b32 s16, s5
	s_branch .LBB0_1201
.LBB0_1200:
	s_or_b64 exec, exec, s[40:41]
	s_add_i32 s16, s16, s30
	v_mov_b64_e32 v[6:7], v[162:163]
	s_cmp_eq_u32 s44, s50
	v_mov_b64_e32 v[8:9], v[164:165]
	v_mov_b32_e32 v235, v236
	s_cbranch_scc1 .LBB0_1197

.LBB0_1205:
	ds_bpermute_b32 v2, v216, v235
	s_mov_b32 s84, s85
	v_mov_b64_e32 v[82:83], s[84:85]
	v_mov_b64_e32 v[84:85], s[86:87]
	v_mov_b64_e32 v[74:75], s[84:85]
	s_waitcnt lgkmcnt(0)
	v_perm_b32 v3, v2, v2, 0
	s_ashr_i32 s17, s16, 31
	v_and_b32_e32 v84, v3, v197
	v_and_b32_e32 v85, v3, v215
	v_mov_b64_e32 v[76:77], s[86:87]
	v_mov_b64_e32 v[80:81], s[90:91]
	v_perm_b32 v3, v2, v2, s0
	s_lshl_b64 s[52:53], s[16:17], 12
	s_ashr_i32 s19, s18, 31
	v_perm_b32 v5, v2, v2, s23
	v_and_b32_e32 v76, v3, v197
	v_and_b32_e32 v77, v3, v215
	v_perm_b32 v81, v2, v2, s1
	v_lshl_add_u64 v[194:195], v[186:187], 0, s[52:53]
	s_lshl_b64 s[52:53], s[18:19], 12
	v_lshl_add_u64 v[2:3], s[42:43], 2, v[188:189]
	v_lshl_add_u64 v[190:191], v[186:187], 0, s[52:53]
	global_load_dword v238, v[194:195], off
	global_load_dword v237, v[190:191], off
	global_load_dwordx2 v[198:199], v[2:3], off
	v_lshl_add_u64 v[2:3], s[40:41], 2, v[188:189]
	s_lshl_b64 s[40:41], s[16:17], 2
	s_add_u32 s42, s36, s40
	s_addc_u32 s43, s37, s41
	global_load_dword v200, v4, s[42:43]
	s_add_u32 s42, s42, s88
	s_addc_u32 s43, s43, s89
	global_load_dwordx2 v[192:193], v[2:3], off
	global_load_dword v196, v4, s[42:43]
	v_mov_b64_e32 v[86:87], s[88:89]
	v_mov_b64_e32 v[88:89], s[90:91]
	v_mov_b64_e32 v[78:79], s[88:89]
	v_mov_b32_e32 v86, s85
	v_mov_b32_e32 v87, s85
	v_and_b32_e32 v88, v5, v197
	v_mov_b32_e32 v78, s85
	v_mov_b32_e32 v79, s85
	v_and_b32_e32 v80, v81, v197
	ds_bpermute_b32 v2, v219, v6
	ds_bpermute_b32 v3, v219, v7
	ds_bpermute_b32 v89, v219, v8
	ds_bpermute_b32 v90, v219, v9
	s_waitcnt lgkmcnt(3)
	v_lshl_or_b32 v2, v2, 7, v218
	s_waitcnt lgkmcnt(2)
	v_lshl_or_b32 v3, v3, 7, v218
	global_load_dwordx4 v[154:157], v2, s[14:15]
	global_load_dwordx4 v[158:161], v3, s[14:15]
	ds_bpermute_b32 v3, v225, v6
	s_waitcnt lgkmcnt(2)
	v_lshl_or_b32 v2, v89, 7, v218
	s_waitcnt lgkmcnt(1)
	v_lshl_or_b32 v89, v90, 7, v218
	ds_bpermute_b32 v90, v225, v7
	global_load_dwordx4 v[146:149], v2, s[14:15]
	global_load_dwordx4 v[150:153], v89, s[14:15]
	s_waitcnt lgkmcnt(1)
	v_lshl_or_b32 v2, v3, 7, v218
	ds_bpermute_b32 v3, v225, v8
	s_waitcnt lgkmcnt(1)
	v_lshl_or_b32 v89, v90, 7, v218
	ds_bpermute_b32 v90, v225, v9
	global_load_dwordx4 v[138:141], v2, s[14:15]
	global_load_dwordx4 v[142:145], v89, s[14:15]
	s_waitcnt lgkmcnt(1)
	v_lshl_or_b32 v2, v3, 7, v218
	ds_bpermute_b32 v3, v226, v6
	s_waitcnt lgkmcnt(1)
	v_lshl_or_b32 v89, v90, 7, v218
	ds_bpermute_b32 v90, v226, v7
	global_load_dwordx4 v[122:125], v2, s[14:15]
	global_load_dwordx4 v[126:129], v89, s[14:15]
	s_waitcnt lgkmcnt(1)
	v_lshl_or_b32 v2, v3, 7, v218
	ds_bpermute_b32 v3, v226, v8
	ds_bpermute_b32 v7, v227, v7
	s_waitcnt lgkmcnt(2)
	v_lshl_or_b32 v89, v90, 7, v218
	ds_bpermute_b32 v90, v226, v9
	global_load_dwordx4 v[114:117], v2, s[14:15]
	global_load_dwordx4 v[118:121], v89, s[14:15]
	s_waitcnt lgkmcnt(2)
	v_lshl_or_b32 v2, v3, 7, v218
	ds_bpermute_b32 v3, v227, v6
	s_waitcnt lgkmcnt(2)
	v_lshl_or_b32 v7, v7, 7, v218
	s_waitcnt lgkmcnt(1)
	v_lshl_or_b32 v6, v90, 7, v218
	global_load_dwordx4 v[106:109], v2, s[14:15]
	global_load_dwordx4 v[110:113], v6, s[14:15]
	ds_bpermute_b32 v6, v227, v9
	s_waitcnt lgkmcnt(1)
	v_lshl_or_b32 v2, v3, 7, v218
	ds_bpermute_b32 v3, v227, v8
	global_load_dwordx4 v[98:101], v2, s[14:15]
	global_load_dwordx4 v[102:105], v7, s[14:15]
	s_waitcnt lgkmcnt(0)
	v_lshl_or_b32 v2, v3, 7, v218
	v_lshl_or_b32 v3, v6, 7, v218
	global_load_dwordx4 v[90:93], v2, s[14:15]
	global_load_dwordx4 v[94:97], v3, s[14:15]
	v_and_b32_e32 v7, v5, v215
	v_mov_b32_e32 v2, v84
	v_mov_b32_e32 v3, v85
	v_mov_b32_e32 v5, v4
	v_mov_b32_e32 v6, v88
	v_mov_b32_e32 v8, v4
	v_mov_b32_e32 v9, v4
	v_mov_b32_e32 v89, v7
	v_mov_b32_e32 v136, v4
	s_waitcnt vmcnt(24)
	v_mfma_scale_f32_16x16x128_f8f6f4 v[130:133], v[58:65], v[2:9], 0, v1, v1 op_sel_hi:[0,0,0]
	v_and_b32_e32 v7, v81, v215
	v_mov_b32_e32 v2, v76
	v_mov_b32_e32 v3, v77
	v_mov_b32_e32 v6, v80
	v_mov_b32_e32 v81, v7
	v_mov_b32_e32 v137, v4
	v_mfma_scale_f32_16x16x128_f8f6f4 v[58:61], v[58:65], v[82:89], 0, v1, v1 op_sel_hi:[0,0,0]
	v_mfma_scale_f32_16x16x128_f8f6f4 v[132:135], v[50:57], v[2:9], v[130:133], v1, v1 op_sel_hi:[0,0,0]
	s_nop 6
	ds_bpermute_b32 v130, v222, v235
	v_mfma_scale_f32_16x16x128_f8f6f4 v[50:53], v[50:57], v[74:81], v[58:61], v1, v1 op_sel_hi:[0,0,0]
	s_waitcnt lgkmcnt(0)
	v_perm_b32 v3, v130, v130, 0
	v_perm_b32 v5, v130, v130, s23
	v_and_b32_e32 v2, v3, v197
	v_and_b32_e32 v3, v3, v215
	v_and_b32_e32 v6, v5, v197
	v_and_b32_e32 v7, v5, v215
	v_mov_b32_e32 v5, v4
	v_perm_b32 v54, v130, v130, s0
	v_perm_b32 v58, v130, v130, s1
	v_and_b32_e32 v130, v54, v197
	v_and_b32_e32 v131, v54, v215
	v_mfma_scale_f32_16x16x128_f8f6f4 v[54:57], v[42:49], v[2:9], v[132:135], v1, v1 op_sel_hi:[0,0,0]
	v_mov_b32_e32 v84, v2
	v_mov_b32_e32 v85, v3
	v_mov_b32_e32 v88, v6
	v_mov_b32_e32 v89, v7
	v_mov_b32_e32 v76, v130
	s_nop 1
	v_and_b32_e32 v134, v58, v197
	v_and_b32_e32 v135, v58, v215
	v_mov_b32_e32 v132, v4
	v_mov_b32_e32 v133, v4
	v_mfma_scale_f32_16x16x128_f8f6f4 v[42:45], v[42:49], v[82:89], v[50:53], v1, v1 op_sel_hi:[0,0,0]
	ds_bpermute_b32 v58, v223, v235
	v_mov_b32_e32 v77, v131
	v_mov_b32_e32 v80, v134
	v_mov_b32_e32 v81, v135
	s_waitcnt lgkmcnt(0)
	v_perm_b32 v3, v58, v58, 0
	v_perm_b32 v7, v58, v58, s23
	v_mfma_scale_f32_16x16x128_f8f6f4 v[46:49], v[34:41], v[130:137], v[54:57], v1, v1 op_sel_hi:[0,0,0]
	v_and_b32_e32 v2, v3, v197
	v_and_b32_e32 v3, v3, v215
	v_and_b32_e32 v6, v7, v197
	v_and_b32_e32 v7, v7, v215
	v_mov_b32_e32 v84, v2
	v_mov_b32_e32 v85, v3
	v_mov_b32_e32 v88, v6
	v_mfma_scale_f32_16x16x128_f8f6f4 v[34:37], v[34:41], v[74:81], v[42:45], v1, v1 op_sel_hi:[0,0,0]
	v_perm_b32 v38, v58, v58, s0
	v_perm_b32 v39, v58, v58, s1
	v_and_b32_e32 v130, v38, v197
	v_and_b32_e32 v131, v38, v215
	v_and_b32_e32 v134, v39, v197
	v_and_b32_e32 v135, v39, v215
	s_nop 0
	ds_bpermute_b32 v42, v224, v235
	v_mfma_scale_f32_16x16x128_f8f6f4 v[38:41], v[26:33], v[2:9], v[46:49], v1, v1 op_sel_hi:[0,0,0]
	v_mov_b32_e32 v89, v7
	v_mov_b32_e32 v76, v130
	v_mov_b32_e32 v77, v131
	v_mov_b32_e32 v80, v134
	v_mov_b32_e32 v81, v135
	s_waitcnt lgkmcnt(0)
	v_perm_b32 v3, v42, v42, 0
	v_perm_b32 v7, v42, v42, s23
	v_mfma_scale_f32_16x16x128_f8f6f4 v[26:29], v[26:33], v[82:89], v[34:37], v1, v1 op_sel_hi:[0,0,0]
	v_and_b32_e32 v2, v3, v197
	v_and_b32_e32 v3, v3, v215
	v_and_b32_e32 v6, v7, v197
	v_and_b32_e32 v7, v7, v215
	v_mov_b32_e32 v85, v3
	s_nop 1
	v_perm_b32 v34, v42, v42, s0
	s_waitcnt vmcnt(23)
	ds_bpermute_b32 v36, v216, v163
	v_mfma_scale_f32_16x16x128_f8f6f4 v[30:33], v[18:25], v[130:137], v[38:41], v1, v1 op_sel_hi:[0,0,0]
	v_and_b32_e32 v130, v34, v197
	v_and_b32_e32 v131, v34, v215
	ds_bpermute_b32 v34, v216, v162
	v_mov_b32_e32 v84, v2
	v_mov_b32_e32 v88, v6
	v_mov_b32_e32 v89, v7
	v_perm_b32 v35, v42, v42, s1
	v_mfma_scale_f32_16x16x128_f8f6f4 v[18:21], v[18:25], v[74:81], v[26:29], v1, v1 op_sel_hi:[0,0,0]
	s_waitcnt lgkmcnt(0)
	v_lshl_or_b32 v22, v34, 7, v218
	v_lshl_or_b32 v23, v36, 7, v218
	global_load_dwordx4 v[58:61], v22, s[14:15]
	global_load_dwordx4 v[62:65], v23, s[14:15]
	v_and_b32_e32 v134, v35, v197
	s_nop 0
	ds_bpermute_b32 v26, v216, v164
	ds_bpermute_b32 v27, v216, v165
	v_and_b32_e32 v135, v35, v215
	v_mfma_scale_f32_16x16x128_f8f6f4 v[22:25], v[10:17], v[2:9], v[30:33], v1, v1 op_sel_hi:[0,0,0]
	ds_bpermute_b32 v3, v222, v162
	s_waitcnt lgkmcnt(2)
	v_lshl_or_b32 v2, v26, 7, v218
	s_waitcnt lgkmcnt(1)
	v_lshl_or_b32 v6, v27, 7, v218
	ds_bpermute_b32 v7, v222, v163
	global_load_dwordx4 v[50:53], v2, s[14:15]
	global_load_dwordx4 v[54:57], v6, s[14:15]
	s_waitcnt lgkmcnt(1)
	v_lshl_or_b32 v2, v3, 7, v218
	ds_bpermute_b32 v3, v222, v164
	v_mfma_scale_f32_16x16x128_f8f6f4 v[208:211], v[10:17], v[82:89], v[18:21], v1, v1 op_sel_hi:[0,0,0]
	s_waitcnt lgkmcnt(1)
	v_lshl_or_b32 v6, v7, 7, v218
	ds_bpermute_b32 v7, v222, v165
	global_load_dwordx4 v[42:45], v2, s[14:15]
	global_load_dwordx4 v[46:49], v6, s[14:15]
	s_waitcnt lgkmcnt(1)
	v_lshl_or_b32 v2, v3, 7, v218
	ds_bpermute_b32 v3, v223, v162
	v_mov_b32_e32 v76, v130
	s_waitcnt lgkmcnt(1)
	v_lshl_or_b32 v6, v7, 7, v218
	ds_bpermute_b32 v7, v223, v163
	global_load_dwordx4 v[34:37], v2, s[14:15]
	global_load_dwordx4 v[38:41], v6, s[14:15]
	s_waitcnt lgkmcnt(1)
	v_lshl_or_b32 v2, v3, 7, v218
	ds_bpermute_b32 v3, v223, v164
	v_mfma_scale_f32_16x16x128_f8f6f4 v[240:243], v[166:173], v[130:137], v[22:25], v1, v1 op_sel_hi:[0,0,0]
	s_waitcnt lgkmcnt(1)
	v_lshl_or_b32 v6, v7, 7, v218
	ds_bpermute_b32 v7, v223, v165
	global_load_dwordx4 v[26:29], v2, s[14:15]
	global_load_dwordx4 v[30:33], v6, s[14:15]
	s_waitcnt lgkmcnt(1)
	v_lshl_or_b32 v2, v3, 7, v218
	ds_bpermute_b32 v3, v224, v162
	v_mov_b32_e32 v77, v131
	s_waitcnt lgkmcnt(1)
	v_lshl_or_b32 v6, v7, 7, v218
	ds_bpermute_b32 v7, v224, v163
	global_load_dwordx4 v[18:21], v2, s[14:15]
	global_load_dwordx4 v[22:25], v6, s[14:15]
	s_waitcnt lgkmcnt(1)
	v_lshl_or_b32 v2, v3, 7, v218
	ds_bpermute_b32 v3, v224, v164
	ds_bpermute_b32 v6, v224, v165
	s_waitcnt lgkmcnt(2)
	v_lshl_or_b32 v7, v7, 7, v218
	global_load_dwordx4 v[10:13], v2, s[14:15]
	global_load_dwordx4 v[14:17], v7, s[14:15]
	v_mov_b32_e32 v80, v134
	s_waitcnt lgkmcnt(1)
	v_lshl_or_b32 v2, v3, 7, v218
	s_waitcnt lgkmcnt(0)
	v_lshl_or_b32 v3, v6, 7, v218
	v_mov_b32_e32 v81, v135
	s_nop 1
	v_mfma_scale_f32_16x16x128_f8f6f4 v[66:69], v[166:173], v[74:81], v[208:211], v1, v1 op_sel_hi:[0,0,0]
	global_load_dwordx4 v[166:169], v2, s[14:15]
	global_load_dwordx4 v[170:173], v3, s[14:15]
	ds_bpermute_b32 v76, v219, v235
	s_waitcnt lgkmcnt(0)
	v_perm_b32 v3, v76, v76, 0
	v_perm_b32 v7, v76, v76, s23
	v_and_b32_e32 v2, v3, v197
	v_and_b32_e32 v3, v3, v215
	v_and_b32_e32 v6, v7, v197
	v_and_b32_e32 v7, v7, v215
	v_mov_b32_e32 v84, v2
	v_mov_b32_e32 v85, v3
	v_mov_b32_e32 v88, v6
	v_mov_b32_e32 v89, v7
	s_waitcnt vmcnt(30)
	v_mfma_scale_f32_16x16x128_f8f6f4 v[70:73], v[154:161], v[2:9], v[240:243], v1, v1 op_sel_hi:[0,0,0]
	v_perm_b32 v2, v76, v76, s0
	v_perm_b32 v3, v76, v76, s1
	v_and_b32_e32 v130, v2, v197
	v_and_b32_e32 v131, v2, v215
	v_and_b32_e32 v134, v3, v197
	v_and_b32_e32 v135, v3, v215
	v_mov_b32_e32 v76, v130
	v_mfma_scale_f32_16x16x128_f8f6f4 v[66:69], v[154:161], v[82:89], v[66:69], v1, v1 op_sel_hi:[0,0,0]
	v_mov_b32_e32 v77, v131
	v_mov_b32_e32 v80, v134
	v_mov_b32_e32 v81, v135
	s_waitcnt vmcnt(28)
	v_mfma_scale_f32_16x16x128_f8f6f4 v[70:73], v[146:153], v[130:137], v[70:73], v1, v1 op_sel_hi:[0,0,0]
	v_mfma_scale_f32_16x16x128_f8f6f4 v[66:69], v[146:153], v[74:81], v[66:69], v1, v1 op_sel_hi:[0,0,0]
	ds_bpermute_b32 v76, v225, v235
	s_waitcnt lgkmcnt(0)
	v_perm_b32 v3, v76, v76, 0
	v_perm_b32 v7, v76, v76, s23
	v_and_b32_e32 v2, v3, v197
	v_and_b32_e32 v3, v3, v215
	v_and_b32_e32 v6, v7, v197
	v_and_b32_e32 v7, v7, v215
	v_mov_b32_e32 v84, v2
	v_mov_b32_e32 v85, v3
	v_mov_b32_e32 v88, v6
	v_mov_b32_e32 v89, v7
	s_waitcnt vmcnt(26)
	v_mfma_scale_f32_16x16x128_f8f6f4 v[70:73], v[138:145], v[2:9], v[70:73], v1, v1 op_sel_hi:[0,0,0]
	v_perm_b32 v2, v76, v76, s0
	v_perm_b32 v3, v76, v76, s1
	v_and_b32_e32 v130, v2, v197
	v_and_b32_e32 v131, v2, v215
	v_and_b32_e32 v134, v3, v197
	v_and_b32_e32 v135, v3, v215
	v_mov_b32_e32 v76, v130
	v_mfma_scale_f32_16x16x128_f8f6f4 v[66:69], v[138:145], v[82:89], v[66:69], v1, v1 op_sel_hi:[0,0,0]
	v_mov_b32_e32 v77, v131
	v_mov_b32_e32 v80, v134
	v_mov_b32_e32 v81, v135
	s_waitcnt vmcnt(24)
	v_mfma_scale_f32_16x16x128_f8f6f4 v[70:73], v[122:129], v[130:137], v[70:73], v1, v1 op_sel_hi:[0,0,0]
	v_mfma_scale_f32_16x16x128_f8f6f4 v[66:69], v[122:129], v[74:81], v[66:69], v1, v1 op_sel_hi:[0,0,0]
	ds_bpermute_b32 v76, v226, v235
	s_waitcnt lgkmcnt(0)
	v_perm_b32 v3, v76, v76, 0
	v_perm_b32 v7, v76, v76, s23
	v_and_b32_e32 v2, v3, v197
	v_and_b32_e32 v3, v3, v215
	v_and_b32_e32 v6, v7, v197
	v_and_b32_e32 v7, v7, v215
	v_mov_b32_e32 v84, v2
	v_mov_b32_e32 v85, v3
	v_mov_b32_e32 v88, v6
	v_mov_b32_e32 v89, v7
	s_waitcnt vmcnt(22)
	v_mfma_scale_f32_16x16x128_f8f6f4 v[70:73], v[114:121], v[2:9], v[70:73], v1, v1 op_sel_hi:[0,0,0]
	v_perm_b32 v2, v76, v76, s0
	v_perm_b32 v3, v76, v76, s1
	v_and_b32_e32 v130, v2, v197
	v_and_b32_e32 v131, v2, v215
	v_and_b32_e32 v134, v3, v197
	v_and_b32_e32 v135, v3, v215
	v_mov_b32_e32 v76, v130
	v_mfma_scale_f32_16x16x128_f8f6f4 v[66:69], v[114:121], v[82:89], v[66:69], v1, v1 op_sel_hi:[0,0,0]
	v_mov_b32_e32 v77, v131
	v_mov_b32_e32 v80, v134
	v_mov_b32_e32 v81, v135
	s_waitcnt vmcnt(20)
	v_mfma_scale_f32_16x16x128_f8f6f4 v[70:73], v[106:113], v[130:137], v[70:73], v1, v1 op_sel_hi:[0,0,0]
	v_mfma_scale_f32_16x16x128_f8f6f4 v[66:69], v[106:113], v[74:81], v[66:69], v1, v1 op_sel_hi:[0,0,0]
	ds_bpermute_b32 v76, v227, v235
	s_waitcnt lgkmcnt(0)
	v_perm_b32 v3, v76, v76, 0
	v_perm_b32 v7, v76, v76, s23
	v_and_b32_e32 v2, v3, v197
	v_and_b32_e32 v3, v3, v215
	v_and_b32_e32 v6, v7, v197
	v_and_b32_e32 v7, v7, v215
	v_mov_b32_e32 v84, v2
	v_mov_b32_e32 v85, v3
	v_mov_b32_e32 v88, v6
	v_mov_b32_e32 v89, v7
	s_waitcnt vmcnt(18)
	v_mfma_scale_f32_16x16x128_f8f6f4 v[70:73], v[98:105], v[2:9], v[70:73], v1, v1 op_sel_hi:[0,0,0]
	v_perm_b32 v2, v76, v76, s0
	v_perm_b32 v3, v76, v76, s1
	v_and_b32_e32 v130, v2, v197
	v_and_b32_e32 v131, v2, v215
	v_and_b32_e32 v134, v3, v197
	v_and_b32_e32 v135, v3, v215
	v_mov_b32_e32 v76, v130
	v_mfma_scale_f32_16x16x128_f8f6f4 v[6:9], v[98:105], v[82:89], v[66:69], v1, v1 op_sel_hi:[0,0,0]
	v_mov_b32_e32 v77, v131
	v_mov_b32_e32 v80, v134
	v_mov_b32_e32 v81, v135
	v_lshlrev_b32_e32 v2, 16, v238
	v_and_b32_e32 v3, 0xffff0000, v238
	s_waitcnt vmcnt(16)
	v_mfma_scale_f32_16x16x128_f8f6f4 v[66:69], v[90:97], v[130:137], v[70:73], v1, v1 op_sel_hi:[0,0,0]
	v_mfma_scale_f32_16x16x128_f8f6f4 v[6:9], v[90:97], v[74:81], v[6:9], v1, v1 op_sel_hi:[0,0,0]
	s_nop 10
	ds_write_b32 v220, v66
	ds_write_b32 v228, v6
	ds_write_b32 v229, v67
	ds_write_b32 v230, v7
	ds_write_b32 v231, v68
	ds_write_b32 v232, v8
	ds_write_b32 v233, v69
	ds_write_b32 v234, v9
	s_waitcnt lgkmcnt(0)
	ds_read2st64_b64 v[6:9], v221 offset1:1
	v_pk_add_f32 v[66:67], v[184:185], v[198:199]
	s_waitcnt lgkmcnt(0)
	s_waitcnt lgkmcnt(0)
	v_pk_mul_f32 v[6:7], v[200:201], v[6:7] op_sel_hi:[0,1]
	v_pk_fma_f32 v[2:3], v[66:67], v[6:7], v[2:3]
	s_nop 0
	v_bfe_u32 v5, v2, 16, 1
	v_add3_u32 v2, v2, v5, s34
	v_bfe_u32 v5, v3, 16, 1
	v_add3_u32 v3, v3, v5, s34
	v_and_b32_e32 v3, 0xffff0000, v3
	v_or_b32_sdwa v5, v3, v2 dst_sel:DWORD dst_unused:UNUSED_PAD src0_sel:DWORD src1_sel:WORD_1
	v_and_b32_e32 v2, 0xffff0000, v2
	v_mul_f32_e32 v3, v3, v3
	v_fmac_f32_e32 v3, v2, v2
	global_store_dword v[194:195], v5, off
	s_nop 0
	v_add_f32_dpp v2, v3, v3 quad_perm:[1,0,3,2] row_mask:0xf bank_mask:0xf bound_ctrl:1
	s_nop 1
	v_add_f32_dpp v2, v2, v2 quad_perm:[2,3,0,1] row_mask:0xf bank_mask:0xf bound_ctrl:1
	s_nop 1
	v_add_f32_dpp v2, v2, v2 row_half_mirror row_mask:0xf bank_mask:0xf bound_ctrl:1
	s_nop 1
	v_add_f32_dpp v2, v2, v2 row_mirror row_mask:0xf bank_mask:0xf bound_ctrl:1
	v_mov_b32_e32 v3, v2
	s_nop 1
	v_permlane16_swap_b32_e32 v2, v3
	v_add_f32_e32 v2, v2, v3
	v_mov_b32_e32 v3, v2
	s_nop 1
	v_permlane32_swap_b32_e32 v2, v3
	s_and_saveexec_b64 s[42:43], s[38:39]
	s_cbranch_execz .LBB0_1207
	s_add_u32 s40, s48, s40
	s_addc_u32 s41, s49, s41
	v_add_f32_e32 v2, v2, v3
	global_store_dword v4, v2, s[40:41]
